# static s_setprio 1 for waves 4-7 at kernel entry (no other setprio left)
# speedup vs baseline: 1.0071x; 1.0071x over previous
; #define LAS __attribute__((address_space(3)))
; __device__ __forceinline__ int lane_id() { unsigned z = 0u; asm volatile("" : "+v"(z)); return (int)__builtin_amdgcn_mbcnt_hi(~0u, __builtin_amdgcn_mbcnt_lo(~0u, z)); }
; __device__ __forceinline__ void s5_precompute_group(const Ctx& c, int g) {
;     LAS float* AR = (LAS float*)c.lds; LAS float* AI = AR + 64; LAS float* BBR = AI + 64; LAS float* BBI = BBR + 1024;
;     LAS float* PR = BBI + 1024; LAS float* PI = PR + 33 * 64; LAS float* CRE = PI + 33 * 64; LAS float* CIM = CRE + 1024;
;     const int tid = c.tid;
;     if (tid < 64) {
;         const int p = tid, i = g * 64 + p;
;         const float dt = expf(c.in[11][g]), lr = c.in[9][i], li = c.in[10][i];
;         const float mag = expf(lr * dt), ar = mag * cosf(li * dt), ai = mag * sinf(li * dt);
;         const float den = lr * lr + li * li;
;         const float cr = ((ar - 1.0f) * lr + ai * li) / den, ci = (ai * lr - (ar - 1.0f) * li) / den;
;         AR[p] = ar; AI[p] = ai;
;         for (int ch = 0; ch < 16; ++ch) { const float br = c.in[12][(size_t)i * 16 + ch], bi = c.in[13][(size_t)i * 16 + ch]; BBR[p * 16 + ch] = cr * br - ci * bi; BBI[p * 16 + ch] = cr * bi + ci * br; }
;         float pr = 1.0f, pi = 0.0f; PR[p] = pr; PI[p] = pi;
;         for (int tau = 1; tau <= 32; ++tau) { const float nr = pr * ar - pi * ai, ni = pr * ai + pi * ar; pr = nr; pi = ni; PR[tau * 64 + p] = pr; PI[tau * 64 + p] = pi; }
;         float* A32 = WSP(float, WS_S5A32) + (size_t)i * 2; A32[0] = pr; A32[1] = pi;
;         *(u32x4*)(WSP(bf16, WS_S5ZERO) + (size_t)g * 512 + p * 8) = (u32x4){0u, 0u, 0u, 0u};
;     }
; __global__ void __launch_bounds__(NTHR, 2) mk_fwd(Args args) {
;     ...
;     c.wave = __builtin_amdgcn_readfirstlane((int)threadIdx.x >> 6); c.lane = lane_id(); c.tid = c.wave * 64 + c.lane;     c.G = gridDim.x; c.bid = blockIdx.x;
;     const int lo = args.ph_lo, hi = args.ph_hi;
;     volatile LAS unsigned* st = (volatile LAS unsigned*)(c.lds + MISC_OFF);
;     if (c.tid < 4) st[c.tid] = 0u;
;     __syncthreads();
;     XcdBarrier bar; bar.bar = WSP(unsigned, WS_CTL) + CW_BAR; bar.x = 0; bar.st = st;
;     if (hi - lo > 1) bar = xcd_barrier_post(WSP(unsigned, WS_CTL) + CW_BAR, st, c.tid == 0);
;     ...
;     if (IN(0)) { ph_prologue(c); if (PROBE_DUP & (1 << 0)) { __syncthreads(); ph_prologue(c); } }
.LBB0_7:
	v_readlane_b32 s0, v254, 4
	s_lshr_b32 s0, s0, 6
	s_cmp_ge_u32 s0, 4
	s_cbranch_scc0 .Lprio_skip
	s_setprio 1
.Lprio_skip:
	s_nop 0
	v_writelane_b32 v254, s0, 46
	s_nop 0
	v_readlane_b32 s4, v254, 5
	v_readlane_b32 s5, v254, 6
	s_cmp_lt_i32 s4, 1
	s_cselect_b64 s[0:1], -1, 0
	s_cmp_gt_i32 s5, 0
	s_cselect_b64 s[4:5], -1, 0
	s_and_b64 s[48:49], s[0:1], s[4:5]
	s_andn2_b64 vcc, exec, s[48:49]
	s_cbranch_vccnz .LBB0_196
	s_cmpk_lt_i32 s2, 0x80
	s_cselect_b64 s[0:1], -1, 0
	s_cmpk_gt_i32 s2, 0x7f
	v_writelane_b32 v254, s0, 47
	s_cselect_b64 s[76:77], -1, 0
	s_and_b64 vcc, exec, s[76:77]
	v_writelane_b32 v254, s1, 48
	v_lshlrev_b32_e32 v0, 3, v1
	s_cbranch_vccnz .LBB0_51
	v_lshl_add_u32 v4, v8, 2, 0
	v_and_b32_e32 v2, 63, v1
	v_mov_b32_e32 v3, 0
	v_mad_u64_u32 v[6:7], s[4:5], v8, 60, v[4:5]
	v_and_b32_e32 v5, 15, v1
	v_lshlrev_b32_e32 v2, 4, v2
	v_lshl_add_u64 v[14:15], s[46:47], 0, v[2:3]
	v_lshlrev_b32_e32 v2, 4, v5
	s_movk_i32 s3, 0xffc4
	v_lshlrev_b32_e32 v12, 3, v8
	v_lshl_add_u64 v[16:17], s[46:47], 0, v[2:3]
	v_max_i32_e32 v2, 0x200, v8
	v_mad_u64_u32 v[10:11], s[4:5], v8, s3, v[6:7]
	s_add_u32 s30, s46, 0x6a280000
	v_ashrrev_i32_e32 v13, 31, v12
	v_sub_u32_e32 v2, v2, v8
	s_addc_u32 s31, s47, 0
	v_lshl_add_u64 v[12:13], v[12:13], 1, s[46:47]
	s_mov_b64 s[4:5], 0x6a200000
	s_movk_i32 s3, 0x400
	v_add_u32_e32 v2, 0x1ff, v2
	v_lshl_add_u64 v[12:13], v[12:13], 0, s[4:5]
	v_cmp_gt_i32_e64 s[4:5], s3, v8
	s_add_u32 s34, s46, 0x67e00000
	s_movk_i32 s3, 0x2000
	v_lshrrev_b32_e32 v9, 9, v2
	v_readlane_b32 s19, v254, 46
	s_addc_u32 s35, s47, 0
	v_cmp_gt_i32_e64 s[6:7], s3, v8
	s_mov_b64 s[10:11], 0x69200000
	s_movk_i32 s3, 0x1ff
	v_add_u32_e32 v18, 1, v9
	s_lshl_b32 s18, s19, 8
	v_lshl_add_u64 v[16:17], v[16:17], 0, s[10:11]
	v_add_u32_e32 v19, -1, v9
	v_cmp_lt_u32_e64 s[10:11], s3, v2
	v_and_b32_e32 v2, 0xfffffe, v18
	s_add_i32 s18, s18, 0
	v_lshrrev_b32_e32 v9, 1, v19
	v_lshl_add_u32 v11, v2, 9, v8
	v_cmp_ne_u32_e64 s[16:17], v18, v2
	v_lshl_add_u32 v2, v1, 2, s18
	v_add_u32_e32 v20, 1, v9
	v_add_u32_e32 v26, 0x6400, v2
	v_lshl_add_u32 v2, v5, 2, 0
	v_lshlrev_b32_e32 v7, 5, v1
	s_mov_b64 s[8:9], 0x68200000
	v_and_b32_e32 v24, 3, v20
	v_add_u32_e32 v27, 0x200, v2
	v_lshlrev_b32_e32 v2, 4, v1
	v_cmp_lt_i32_e64 s[0:1], 63, v8
	v_and_b32_e32 v7, 0x7c0, v7
	v_lshl_add_u64 v[14:15], v[14:15], 0, s[8:9]
	v_cmp_gt_u32_e64 s[8:9], 8, v5
	v_add_u32_e32 v9, 0x200, v8
	v_cmp_lt_u32_e64 s[12:13], 5, v19
	v_and_b32_e32 v25, -4, v20
	v_cmp_ne_u32_e64 s[14:15], 0, v24
	v_add_u32_e32 v28, 0xfffffe00, v8
	v_lshl_add_u32 v29, s19, 9, v0
	v_lshl_add_u32 v30, s19, 10, v2
	s_mov_b32 s33, 0x3fb8aa3b
	s_mov_b32 s97, 0xc2ce8ed0
	s_mov_b32 s28, 0x42b17218
	s_mov_b32 s50, 0xfe5163ab
	s_mov_b32 s51, 0x3c439041
	s_mov_b32 s68, 0xdb629599
	s_mov_b32 s69, 0xf534ddc0
	s_mov_b32 s70, 0xfc2757d1
	s_mov_b32 s71, 0x4e441529
	s_mov_b32 s26, 0xa2f9836e
	s_mov_b32 s27, 0x3fc90fda
	s_mov_b32 s24, 0xbfc90fda
	v_mov_b32_e32 v31, 0x3c0881c4
	v_mov_b32_e32 v32, 0xbab64f3b
	v_mov_b32_e32 v33, 1.0
	s_mov_b64 s[36:37], 0x800
	s_add_i32 s25, 0, 0x2200
	s_movk_i32 s29, 0x1dff
	v_mov_b32_e32 v34, 0x7f800000
	v_not_b32_e32 v35, 63
	v_not_b32_e32 v36, 31
	v_mov_b32_e32 v37, 0x7fc00000
	v_mov_b32_e32 v46, v3
	v_mov_b32_e32 v47, v3
	v_mov_b32_e32 v48, v3
	v_mov_b32_e32 v49, v3
	s_mov_b32 s38, s2
	s_branch .LBB0_11
